# w2 conversion in the expert GEMM 1 epilogues spread thinner: 64k x 16n sub-tile (4 loads) per wave in each of the first 16 units
# speedup vs baseline: 1.0429x; 1.0013x over previous
.LBB0_1061:
	v_mov_b32_e32 v2, v243
	s_nop 15
	s_nop 15
	s_lshl_b32 s23, s51, 8
	v_readfirstlane_b32 s21, v2
	s_ashr_i32 s25, s21, 2
	s_andn2_b32 s25, s25, 63
	s_lshr_b32 s21, s21, 1
	s_add_i32 s25, s25, s23
	s_lshl_b32 s23, s76, 7
	s_and_b32 s21, s21, 0x60
	v_and_or_b32 v6, v2, 15, s25
	s_or_b32 s21, s21, s23
	v_lshrrev_b32_e32 v2, 1, v2
	v_and_or_b32 v4, v2, 24, s21
	s_waitcnt vmcnt(8)
	s_mov_b32 s32, 0
	s_cmp_gt_u32 s74, 2
	s_cbranch_scc1 .Lcg_skip_i
	s_cmp_gt_u32 s51, 0x1ff
	s_cbranch_scc1 .Lcg_skip_i
	s_load_dword s101, s[0:1], 0xb0
	s_load_dwordx2 s[80:81], s[0:1], 0x78
	s_load_dwordx2 s[82:83], s[0:1], 0xa0
	v_readlane_b32 s84, v255, 7
	v_readfirstlane_b32 s85, v0
	s_lshr_b32 s85, s85, 6
	s_lshl_b32 s84, s84, 3
	s_add_i32 s84, s84, s85
	s_bfe_u32 s85, s51, 0x30006
	s_lshl_b32 s85, s85, 11
	s_add_i32 s85, s85, s84
	s_lshr_b32 s84, s85, 9
	s_add_i32 s92, s74, 1
	s_lshl_b32 s92, s92, 5
	s_add_i32 s84, s84, s92
	s_lshl_b32 s92, s84, 22
	s_bfe_u32 s93, s85, 0x30006
	s_lshl_b32 s93, s93, 19
	s_add_u32 s92, s92, s93
	s_and_b32 s93, s85, 63
	s_lshl_b32 s93, s93, 6
	s_add_u32 s92, s92, s93
	s_bfe_u32 s93, s51, 0x10005
	s_lshl_b32 s93, s93, 18
	s_add_u32 s100, s92, s93
	s_lshl_b32 s92, s84, 20
	s_and_b32 s93, s85, 63
	s_lshl_b32 s93, s93, 14
	s_add_u32 s92, s92, s93
	s_bfe_u32 s93, s85, 0x30006
	s_lshl_b32 s93, s93, 7
	s_add_u32 s92, s92, s93
	s_bfe_u32 s93, s51, 0x10005
	s_lshl_b32 s93, s93, 6
	s_add_u32 s92, s92, s93
	s_add_u32 s92, s92, 0x21f00000
	s_waitcnt lgkmcnt(0)
	s_cmpk_lg_i32 s101, 0x100
	s_cbranch_scc1 .Lcg_skip_i
	s_add_u32 s80, s80, s100
	s_addc_u32 s81, s81, 0
	s_add_u32 s82, s82, s92
	s_addc_u32 s83, s83, 0
	v_and_b32_e32 v56, 63, v0
	v_lshrrev_b32_e32 v57, 2, v56
	v_and_b32_e32 v56, 3, v56
	v_lshlrev_b32_e32 v57, 14, v57
	v_lshl_or_b32 v56, v56, 4, v57
	global_load_dwordx4 v[24:27], v56, s[80:81] nt
	v_add_u32_e32 v57, 0x1000, v56
	global_load_dwordx4 v[28:31], v57, s[80:81] nt
	v_add_u32_e32 v57, 0x2000, v56
	global_load_dwordx4 v[32:35], v57, s[80:81] nt
	v_add_u32_e32 v57, 0x3000, v56
	global_load_dwordx4 v[36:39], v57, s[80:81] nt
	s_mov_b32 s32, 1
.Lcg_skip_i:
	v_pk_fma_f32 v[2:3], v[210:211], s[50:51], v[78:79] op_sel_hi:[1,0,1]
	v_pk_fma_f32 v[16:17], v[206:207], s[50:51], v[82:83] op_sel_hi:[1,0,1]
	v_min_f32_e32 v2, 0x40e00000, v2
	v_mul_f32_e32 v8, 0xc01d265f, v2
	v_min_f32_e32 v3, 0x40e00000, v3
	v_exp_f32_e32 v10, v8
	v_mul_f32_e32 v8, 0xc01d265f, v3
	v_exp_f32_e32 v11, v8
	v_pk_fma_f32 v[8:9], v[212:213], s[50:51], v[80:81] op_sel_hi:[1,0,1]
	v_add_f32_e32 v10, 1.0, v10
	v_rcp_f32_e32 v10, v10
	v_add_f32_e32 v11, 1.0, v11
	v_rcp_f32_e32 v11, v11
	v_min_f32_e32 v8, 0x40e00000, v8
	v_min_f32_e32 v9, 0x40e00000, v9
	v_mul_f32_e32 v12, 0xc01d265f, v8
	v_mul_f32_e32 v13, 0xc01d265f, v9
	v_exp_f32_e32 v12, v12
	v_exp_f32_e32 v13, v13
	v_med3_f32 v16, v16, s71, v242
	v_med3_f32 v17, v17, s71, v242
	v_pk_fma_f32 v[14:15], v[208:209], s[50:51], v[84:85] op_sel_hi:[1,0,1]
	v_pk_add_f32 v[16:17], v[16:17], 1.0 op_sel_hi:[1,0]
	v_pk_mul_f32 v[2:3], v[2:3], v[10:11]
	v_med3_f32 v14, v14, s71, v242
	v_med3_f32 v15, v15, s71, v242
	v_pk_mul_f32 v[2:3], v[2:3], v[16:17]
	v_mov_b32_e32 v10, v215
	v_cvt_pk_fp8_f32 v10, v2, v3
	v_pk_add_f32 v[2:3], v[14:15], 1.0 op_sel_hi:[1,0]
	v_pk_fma_f32 v[14:15], v[202:203], s[50:51], v[70:71] op_sel_hi:[1,0,1]
	v_add_f32_e32 v12, 1.0, v12
	v_add_f32_e32 v13, 1.0, v13
	v_min_f32_e32 v14, 0x40e00000, v14
	v_rcp_f32_e32 v12, v12
	v_rcp_f32_e32 v13, v13
	v_min_f32_e32 v15, 0x40e00000, v15
	v_mul_f32_e32 v11, 0xc01d265f, v14
	v_exp_f32_e32 v11, v11
	v_mul_f32_e32 v16, 0xc01d265f, v15
	v_exp_f32_e32 v17, v16
	v_pk_mul_f32 v[8:9], v[8:9], v[12:13]
	v_pk_fma_f32 v[12:13], v[204:205], s[50:51], v[72:73] op_sel_hi:[1,0,1]
	v_add_f32_e32 v11, 1.0, v11
	v_min_f32_e32 v12, 0x40e00000, v12
	v_min_f32_e32 v13, 0x40e00000, v13
	v_rcp_f32_e32 v16, v11
	v_add_f32_e32 v11, 1.0, v17
	v_mul_f32_e32 v17, 0xc01d265f, v12
	v_exp_f32_e32 v18, v17
	v_mul_f32_e32 v17, 0xc01d265f, v13
	v_exp_f32_e32 v19, v17
	v_rcp_f32_e32 v17, v11
	v_pk_mul_f32 v[2:3], v[8:9], v[2:3]
	v_pk_fma_f32 v[8:9], v[198:199], s[50:51], v[74:75] op_sel_hi:[1,0,1]
	v_add_f32_e32 v11, 1.0, v18
	v_med3_f32 v8, v8, s71, v242
	v_med3_f32 v9, v9, s71, v242
	v_rcp_f32_e32 v18, v11
	v_add_f32_e32 v11, 1.0, v19
	v_pk_add_f32 v[8:9], v[8:9], 1.0 op_sel_hi:[1,0]
	v_rcp_f32_e32 v19, v11
	v_pk_mul_f32 v[14:15], v[14:15], v[16:17]
	v_mov_b32_e32 v11, v215
	v_pk_mul_f32 v[8:9], v[14:15], v[8:9]
	v_cvt_pk_fp8_f32 v10, v2, v3 op_sel:[0,0,1]
	v_pk_fma_f32 v[2:3], v[200:201], s[50:51], v[76:77] op_sel_hi:[1,0,1]
	v_cvt_pk_fp8_f32 v11, v8, v9
	v_med3_f32 v2, v2, s71, v242
	v_med3_f32 v3, v3, s71, v242
	v_pk_add_f32 v[2:3], v[2:3], 1.0 op_sel_hi:[1,0]
	v_pk_mul_f32 v[8:9], v[12:13], v[18:19]
	v_ashrrev_i32_e32 v7, 31, v6
	v_pk_mul_f32 v[2:3], v[8:9], v[2:3]
	v_ashrrev_i32_e32 v5, 31, v4
	v_cvt_pk_fp8_f32 v11, v2, v3 op_sel:[0,0,1]
	v_lshlrev_b64 v[2:3], 10, v[6:7]
	v_lshl_add_u64 v[2:3], s[14:15], 0, v[2:3]
	v_lshl_add_u64 v[2:3], v[2:3], 0, v[4:5]
	global_store_dwordx2 v[2:3], v[10:11], off
	v_pk_fma_f32 v[10:11], v[194:195], s[50:51], v[78:79] op_sel_hi:[1,0,1]
	v_pk_fma_f32 v[20:21], v[190:191], s[50:51], v[82:83] op_sel_hi:[1,0,1]
	v_min_f32_e32 v10, 0x40e00000, v10
	v_mul_f32_e32 v7, 0xc01d265f, v10
	v_min_f32_e32 v11, 0x40e00000, v11
	v_exp_f32_e32 v7, v7
	v_mul_f32_e32 v12, 0xc01d265f, v11
	v_exp_f32_e32 v15, v12
	v_pk_fma_f32 v[12:13], v[196:197], s[50:51], v[80:81] op_sel_hi:[1,0,1]
	v_add_f32_e32 v7, 1.0, v7
	v_min_f32_e32 v12, 0x40e00000, v12
	v_rcp_f32_e32 v14, v7
	v_add_f32_e32 v7, 1.0, v15
	v_mul_f32_e32 v15, 0xc01d265f, v12
	v_min_f32_e32 v13, 0x40e00000, v13
	v_exp_f32_e32 v16, v15
	v_mul_f32_e32 v15, 0xc01d265f, v13
	v_exp_f32_e32 v17, v15
	v_rcp_f32_e32 v15, v7
	v_med3_f32 v20, v20, s71, v242
	v_med3_f32 v21, v21, s71, v242
	v_pk_fma_f32 v[18:19], v[192:193], s[50:51], v[84:85] op_sel_hi:[1,0,1]
	v_pk_add_f32 v[20:21], v[20:21], 1.0 op_sel_hi:[1,0]
	v_pk_mul_f32 v[10:11], v[10:11], v[14:15]
	v_med3_f32 v18, v18, s71, v242
	v_med3_f32 v19, v19, s71, v242
	v_pk_mul_f32 v[10:11], v[10:11], v[20:21]
	v_mov_b32_e32 v14, v215
	v_add_f32_e32 v7, 1.0, v16
	v_cvt_pk_fp8_f32 v14, v10, v11
	v_pk_add_f32 v[10:11], v[18:19], 1.0 op_sel_hi:[1,0]
	v_pk_fma_f32 v[18:19], v[186:187], s[50:51], v[70:71] op_sel_hi:[1,0,1]
	v_rcp_f32_e32 v16, v7
	v_add_f32_e32 v7, 1.0, v17
	v_min_f32_e32 v18, 0x40e00000, v18
	v_rcp_f32_e32 v17, v7
	v_min_f32_e32 v19, 0x40e00000, v19
	v_mul_f32_e32 v7, 0xc01d265f, v18
	v_exp_f32_e32 v7, v7
	v_mul_f32_e32 v15, 0xc01d265f, v19
	v_exp_f32_e32 v15, v15
	v_pk_mul_f32 v[12:13], v[12:13], v[16:17]
	v_pk_fma_f32 v[16:17], v[188:189], s[50:51], v[72:73] op_sel_hi:[1,0,1]
	v_add_f32_e32 v7, 1.0, v7
	v_min_f32_e32 v16, 0x40e00000, v16
	v_min_f32_e32 v17, 0x40e00000, v17
	v_rcp_f32_e32 v20, v7
	v_add_f32_e32 v7, 1.0, v15
	v_mul_f32_e32 v15, 0xc01d265f, v16
	v_exp_f32_e32 v15, v15
	v_mul_f32_e32 v21, 0xc01d265f, v17
	v_exp_f32_e32 v23, v21
	v_rcp_f32_e32 v21, v7
	v_pk_mul_f32 v[10:11], v[12:13], v[10:11]
	v_pk_fma_f32 v[12:13], v[182:183], s[50:51], v[74:75] op_sel_hi:[1,0,1]
	v_add_f32_e32 v7, 1.0, v15
	v_med3_f32 v12, v12, s71, v242
	v_med3_f32 v13, v13, s71, v242
	v_rcp_f32_e32 v22, v7
	v_add_f32_e32 v7, 1.0, v23
	v_pk_add_f32 v[12:13], v[12:13], 1.0 op_sel_hi:[1,0]
	v_rcp_f32_e32 v23, v7
	v_pk_mul_f32 v[18:19], v[18:19], v[20:21]
	v_mov_b32_e32 v15, v215
	v_pk_mul_f32 v[12:13], v[18:19], v[12:13]
	v_cvt_pk_fp8_f32 v14, v10, v11 op_sel:[0,0,1]
	v_pk_fma_f32 v[10:11], v[184:185], s[50:51], v[76:77] op_sel_hi:[1,0,1]
	v_cvt_pk_fp8_f32 v15, v12, v13
	v_med3_f32 v10, v10, s71, v242
	v_med3_f32 v11, v11, s71, v242
	v_pk_add_f32 v[10:11], v[10:11], 1.0 op_sel_hi:[1,0]
	v_pk_mul_f32 v[12:13], v[16:17], v[22:23]
	v_or_b32_e32 v8, 16, v6
	v_pk_mul_f32 v[10:11], v[12:13], v[10:11]
	v_ashrrev_i32_e32 v9, 31, v8
	v_cvt_pk_fp8_f32 v15, v10, v11 op_sel:[0,0,1]
	v_pk_fma_f32 v[10:11], v[178:179], s[50:51], v[78:79] op_sel_hi:[1,0,1]
	v_lshlrev_b64 v[8:9], 10, v[8:9]
	v_min_f32_e32 v10, 0x40e00000, v10
	v_lshl_add_u64 v[8:9], s[14:15], 0, v[8:9]
	v_mul_f32_e32 v7, 0xc01d265f, v10
	v_min_f32_e32 v11, 0x40e00000, v11
	v_lshl_add_u64 v[8:9], v[8:9], 0, v[4:5]
	v_exp_f32_e32 v7, v7
	v_mul_f32_e32 v12, 0xc01d265f, v11
	global_store_dwordx2 v[8:9], v[14:15], off
	v_exp_f32_e32 v15, v12
	v_pk_fma_f32 v[12:13], v[180:181], s[50:51], v[80:81] op_sel_hi:[1,0,1]
	v_add_f32_e32 v7, 1.0, v7
	v_min_f32_e32 v12, 0x40e00000, v12
	v_rcp_f32_e32 v14, v7
	v_add_f32_e32 v7, 1.0, v15
	v_mul_f32_e32 v15, 0xc01d265f, v12
	v_min_f32_e32 v13, 0x40e00000, v13
	v_exp_f32_e32 v16, v15
	v_mul_f32_e32 v15, 0xc01d265f, v13
	v_exp_f32_e32 v17, v15
	v_rcp_f32_e32 v15, v7
	v_pk_fma_f32 v[20:21], v[174:175], s[50:51], v[82:83] op_sel_hi:[1,0,1]
	v_pk_fma_f32 v[18:19], v[176:177], s[50:51], v[84:85] op_sel_hi:[1,0,1]
	v_med3_f32 v20, v20, s71, v242
	v_med3_f32 v21, v21, s71, v242
	v_pk_add_f32 v[20:21], v[20:21], 1.0 op_sel_hi:[1,0]
	v_pk_mul_f32 v[10:11], v[10:11], v[14:15]
	v_med3_f32 v18, v18, s71, v242
	v_med3_f32 v19, v19, s71, v242
	v_pk_mul_f32 v[10:11], v[10:11], v[20:21]
	v_mov_b32_e32 v14, v215
	v_add_f32_e32 v7, 1.0, v16
	v_cvt_pk_fp8_f32 v14, v10, v11
	v_pk_add_f32 v[10:11], v[18:19], 1.0 op_sel_hi:[1,0]
	v_pk_fma_f32 v[18:19], v[170:171], s[50:51], v[70:71] op_sel_hi:[1,0,1]
	v_rcp_f32_e32 v16, v7
	v_add_f32_e32 v7, 1.0, v17
	v_min_f32_e32 v18, 0x40e00000, v18
	v_rcp_f32_e32 v17, v7
	v_min_f32_e32 v19, 0x40e00000, v19
	v_mul_f32_e32 v7, 0xc01d265f, v18
	v_exp_f32_e32 v7, v7
	v_mul_f32_e32 v15, 0xc01d265f, v19
	v_exp_f32_e32 v15, v15
	v_pk_mul_f32 v[12:13], v[12:13], v[16:17]
	v_pk_fma_f32 v[16:17], v[172:173], s[50:51], v[72:73] op_sel_hi:[1,0,1]
	v_add_f32_e32 v7, 1.0, v7
	v_min_f32_e32 v16, 0x40e00000, v16
	v_min_f32_e32 v17, 0x40e00000, v17
	v_rcp_f32_e32 v20, v7
	v_add_f32_e32 v7, 1.0, v15
	v_mul_f32_e32 v15, 0xc01d265f, v16
	v_exp_f32_e32 v15, v15
	v_mul_f32_e32 v21, 0xc01d265f, v17
	v_exp_f32_e32 v23, v21
	v_rcp_f32_e32 v21, v7
	v_pk_mul_f32 v[10:11], v[12:13], v[10:11]
	v_pk_fma_f32 v[12:13], v[166:167], s[50:51], v[74:75] op_sel_hi:[1,0,1]
	v_add_f32_e32 v7, 1.0, v15
	v_med3_f32 v12, v12, s71, v242
	v_med3_f32 v13, v13, s71, v242
	v_rcp_f32_e32 v22, v7
	v_add_f32_e32 v7, 1.0, v23
	v_pk_add_f32 v[12:13], v[12:13], 1.0 op_sel_hi:[1,0]
	v_rcp_f32_e32 v23, v7
	v_pk_mul_f32 v[18:19], v[18:19], v[20:21]
	v_mov_b32_e32 v15, v215
	v_pk_mul_f32 v[12:13], v[18:19], v[12:13]
	v_cvt_pk_fp8_f32 v14, v10, v11 op_sel:[0,0,1]
	v_pk_fma_f32 v[10:11], v[168:169], s[50:51], v[76:77] op_sel_hi:[1,0,1]
	v_cvt_pk_fp8_f32 v15, v12, v13
	v_med3_f32 v10, v10, s71, v242
	v_med3_f32 v11, v11, s71, v242
	v_pk_add_f32 v[10:11], v[10:11], 1.0 op_sel_hi:[1,0]
	v_pk_mul_f32 v[12:13], v[16:17], v[22:23]
	v_or_b32_e32 v8, 32, v6
	v_pk_mul_f32 v[10:11], v[12:13], v[10:11]
	v_ashrrev_i32_e32 v9, 31, v8
	v_cvt_pk_fp8_f32 v15, v10, v11 op_sel:[0,0,1]
	v_lshlrev_b64 v[8:9], 10, v[8:9]
	v_lshl_add_u64 v[8:9], s[14:15], 0, v[8:9]
	v_lshl_add_u64 v[8:9], v[8:9], 0, v[4:5]
	global_store_dwordx2 v[8:9], v[14:15], off
	v_pk_fma_f32 v[8:9], v[162:163], s[50:51], v[78:79] op_sel_hi:[1,0,1]
	v_pk_fma_f32 v[18:19], v[158:159], s[50:51], v[82:83] op_sel_hi:[1,0,1]
	v_min_f32_e32 v8, 0x40e00000, v8
	v_mul_f32_e32 v10, 0xc01d265f, v8
	v_min_f32_e32 v9, 0x40e00000, v9
	v_exp_f32_e32 v12, v10
	v_mul_f32_e32 v10, 0xc01d265f, v9
	v_exp_f32_e32 v13, v10
	v_pk_fma_f32 v[10:11], v[164:165], s[50:51], v[80:81] op_sel_hi:[1,0,1]
	v_add_f32_e32 v12, 1.0, v12
	v_rcp_f32_e32 v12, v12
	v_add_f32_e32 v13, 1.0, v13
	v_rcp_f32_e32 v13, v13
	v_min_f32_e32 v10, 0x40e00000, v10
	v_min_f32_e32 v11, 0x40e00000, v11
	v_mul_f32_e32 v14, 0xc01d265f, v10
	v_mul_f32_e32 v15, 0xc01d265f, v11
	v_exp_f32_e32 v14, v14
	v_exp_f32_e32 v15, v15
	v_med3_f32 v18, v18, s71, v242
	v_med3_f32 v19, v19, s71, v242
	v_pk_fma_f32 v[16:17], v[160:161], s[50:51], v[84:85] op_sel_hi:[1,0,1]
	v_pk_add_f32 v[18:19], v[18:19], 1.0 op_sel_hi:[1,0]
	v_pk_mul_f32 v[8:9], v[8:9], v[12:13]
	v_med3_f32 v16, v16, s71, v242
	v_med3_f32 v17, v17, s71, v242
	v_pk_mul_f32 v[8:9], v[8:9], v[18:19]
	v_mov_b32_e32 v12, v215
	v_cvt_pk_fp8_f32 v12, v8, v9
	v_pk_add_f32 v[8:9], v[16:17], 1.0 op_sel_hi:[1,0]
	v_pk_fma_f32 v[16:17], v[154:155], s[50:51], v[70:71] op_sel_hi:[1,0,1]
	v_add_f32_e32 v14, 1.0, v14
	v_add_f32_e32 v15, 1.0, v15
	v_min_f32_e32 v16, 0x40e00000, v16
	v_rcp_f32_e32 v14, v14
	v_rcp_f32_e32 v15, v15
	v_min_f32_e32 v17, 0x40e00000, v17
	v_mul_f32_e32 v13, 0xc01d265f, v16
	v_exp_f32_e32 v13, v13
	v_mul_f32_e32 v18, 0xc01d265f, v17
	v_exp_f32_e32 v19, v18
	v_pk_mul_f32 v[10:11], v[10:11], v[14:15]
	v_pk_fma_f32 v[14:15], v[156:157], s[50:51], v[72:73] op_sel_hi:[1,0,1]
	v_add_f32_e32 v13, 1.0, v13
	v_min_f32_e32 v14, 0x40e00000, v14
	v_min_f32_e32 v15, 0x40e00000, v15
	v_rcp_f32_e32 v18, v13
	v_add_f32_e32 v13, 1.0, v19
	v_mul_f32_e32 v19, 0xc01d265f, v14
	v_exp_f32_e32 v20, v19
	v_mul_f32_e32 v19, 0xc01d265f, v15
	v_exp_f32_e32 v21, v19
	v_rcp_f32_e32 v19, v13
	v_pk_mul_f32 v[8:9], v[10:11], v[8:9]
	v_pk_fma_f32 v[10:11], v[150:151], s[50:51], v[74:75] op_sel_hi:[1,0,1]
	v_add_f32_e32 v13, 1.0, v20
	v_med3_f32 v10, v10, s71, v242
	v_med3_f32 v11, v11, s71, v242
	v_rcp_f32_e32 v20, v13
	v_add_f32_e32 v13, 1.0, v21
	v_pk_add_f32 v[10:11], v[10:11], 1.0 op_sel_hi:[1,0]
	v_rcp_f32_e32 v21, v13
	v_pk_mul_f32 v[16:17], v[16:17], v[18:19]
	v_mov_b32_e32 v13, v215
	v_pk_mul_f32 v[10:11], v[16:17], v[10:11]
	v_cvt_pk_fp8_f32 v12, v8, v9 op_sel:[0,0,1]
	v_pk_fma_f32 v[8:9], v[152:153], s[50:51], v[76:77] op_sel_hi:[1,0,1]
	v_cvt_pk_fp8_f32 v13, v10, v11
	v_med3_f32 v8, v8, s71, v242
	v_med3_f32 v9, v9, s71, v242
	v_pk_add_f32 v[8:9], v[8:9], 1.0 op_sel_hi:[1,0]
	v_pk_mul_f32 v[10:11], v[14:15], v[20:21]
	v_or_b32_e32 v6, 48, v6
	v_pk_mul_f32 v[8:9], v[10:11], v[8:9]
	v_ashrrev_i32_e32 v7, 31, v6
	v_cvt_pk_fp8_f32 v13, v8, v9 op_sel:[0,0,1]
	v_lshlrev_b64 v[6:7], 10, v[6:7]
	v_lshl_add_u64 v[6:7], s[14:15], 0, v[6:7]
	v_lshl_add_u64 v[4:5], v[6:7], 0, v[4:5]
	global_store_dwordx2 v[4:5], v[12:13], off
	v_pk_fma_f32 v[4:5], v[146:147], s[50:51], v[78:79] op_sel_hi:[1,0,1]
	v_pk_fma_f32 v[14:15], v[142:143], s[50:51], v[82:83] op_sel_hi:[1,0,1]
	v_min_f32_e32 v4, 0x40e00000, v4
	v_mul_f32_e32 v6, 0xc01d265f, v4
	v_min_f32_e32 v5, 0x40e00000, v5
	v_exp_f32_e32 v8, v6
	v_mul_f32_e32 v6, 0xc01d265f, v5
	v_exp_f32_e32 v9, v6
	v_pk_fma_f32 v[6:7], v[148:149], s[50:51], v[80:81] op_sel_hi:[1,0,1]
	v_add_f32_e32 v8, 1.0, v8
	v_rcp_f32_e32 v8, v8
	v_add_f32_e32 v9, 1.0, v9
	v_rcp_f32_e32 v9, v9
	v_min_f32_e32 v6, 0x40e00000, v6
	v_min_f32_e32 v7, 0x40e00000, v7
	v_mul_f32_e32 v10, 0xc01d265f, v6
	v_mul_f32_e32 v11, 0xc01d265f, v7
	v_exp_f32_e32 v10, v10
	v_exp_f32_e32 v11, v11
	v_med3_f32 v14, v14, s71, v242
	v_med3_f32 v15, v15, s71, v242
	v_pk_fma_f32 v[12:13], v[144:145], s[50:51], v[84:85] op_sel_hi:[1,0,1]
	v_pk_add_f32 v[14:15], v[14:15], 1.0 op_sel_hi:[1,0]
	v_pk_mul_f32 v[4:5], v[4:5], v[8:9]
	v_med3_f32 v12, v12, s71, v242
	v_med3_f32 v13, v13, s71, v242
	v_pk_mul_f32 v[4:5], v[4:5], v[14:15]
	v_mov_b32_e32 v8, v215
	v_cvt_pk_fp8_f32 v8, v4, v5
	v_pk_add_f32 v[4:5], v[12:13], 1.0 op_sel_hi:[1,0]
	v_pk_fma_f32 v[12:13], v[138:139], s[50:51], v[70:71] op_sel_hi:[1,0,1]
	v_add_f32_e32 v10, 1.0, v10
	v_add_f32_e32 v11, 1.0, v11
	v_min_f32_e32 v12, 0x40e00000, v12
	v_rcp_f32_e32 v10, v10
	v_rcp_f32_e32 v11, v11
	v_min_f32_e32 v13, 0x40e00000, v13
	v_mul_f32_e32 v9, 0xc01d265f, v12
	v_exp_f32_e32 v9, v9
	v_mul_f32_e32 v14, 0xc01d265f, v13
	v_exp_f32_e32 v15, v14
	v_pk_mul_f32 v[6:7], v[6:7], v[10:11]
	v_pk_fma_f32 v[10:11], v[140:141], s[50:51], v[72:73] op_sel_hi:[1,0,1]
	v_add_f32_e32 v9, 1.0, v9
	v_min_f32_e32 v10, 0x40e00000, v10
	v_min_f32_e32 v11, 0x40e00000, v11
	v_rcp_f32_e32 v14, v9
	v_add_f32_e32 v9, 1.0, v15
	v_mul_f32_e32 v15, 0xc01d265f, v10
	v_exp_f32_e32 v16, v15
	v_mul_f32_e32 v15, 0xc01d265f, v11
	v_exp_f32_e32 v17, v15
	v_rcp_f32_e32 v15, v9
	v_pk_mul_f32 v[4:5], v[6:7], v[4:5]
	v_pk_fma_f32 v[6:7], v[134:135], s[50:51], v[74:75] op_sel_hi:[1,0,1]
	v_add_f32_e32 v9, 1.0, v16
	v_med3_f32 v6, v6, s71, v242
	v_med3_f32 v7, v7, s71, v242
	v_rcp_f32_e32 v16, v9
	v_add_f32_e32 v9, 1.0, v17
	v_pk_add_f32 v[6:7], v[6:7], 1.0 op_sel_hi:[1,0]
	v_rcp_f32_e32 v17, v9
	v_pk_mul_f32 v[12:13], v[12:13], v[14:15]
	v_mov_b32_e32 v9, v215
	v_pk_mul_f32 v[6:7], v[12:13], v[6:7]
	v_cvt_pk_fp8_f32 v8, v4, v5 op_sel:[0,0,1]
	v_pk_fma_f32 v[4:5], v[136:137], s[50:51], v[76:77] op_sel_hi:[1,0,1]
	v_cvt_pk_fp8_f32 v9, v6, v7
	v_med3_f32 v4, v4, s71, v242
	v_med3_f32 v5, v5, s71, v242
	v_pk_add_f32 v[4:5], v[4:5], 1.0 op_sel_hi:[1,0]
	v_pk_mul_f32 v[6:7], v[10:11], v[16:17]
	v_pk_fma_f32 v[14:15], v[126:127], s[50:51], v[82:83] op_sel_hi:[1,0,1]
	v_pk_mul_f32 v[4:5], v[6:7], v[4:5]
	v_med3_f32 v14, v14, s71, v242
	v_cvt_pk_fp8_f32 v9, v4, v5 op_sel:[0,0,1]
	v_add_co_u32_e32 v4, vcc, s2, v2
	v_med3_f32 v15, v15, s71, v242
	s_nop 0
	v_addc_co_u32_e32 v5, vcc, 0, v3, vcc
	global_store_dwordx2 v[4:5], v[8:9], off
	v_pk_fma_f32 v[4:5], v[130:131], s[50:51], v[78:79] op_sel_hi:[1,0,1]
	v_pk_fma_f32 v[12:13], v[128:129], s[50:51], v[84:85] op_sel_hi:[1,0,1]
	v_min_f32_e32 v4, 0x40e00000, v4
	v_mul_f32_e32 v6, 0xc01d265f, v4
	v_min_f32_e32 v5, 0x40e00000, v5
	v_exp_f32_e32 v8, v6
	v_mul_f32_e32 v6, 0xc01d265f, v5
	v_exp_f32_e32 v9, v6
	v_pk_fma_f32 v[6:7], v[132:133], s[50:51], v[80:81] op_sel_hi:[1,0,1]
	v_add_f32_e32 v8, 1.0, v8
	v_rcp_f32_e32 v8, v8
	v_add_f32_e32 v9, 1.0, v9
	v_rcp_f32_e32 v9, v9
	v_min_f32_e32 v6, 0x40e00000, v6
	v_min_f32_e32 v7, 0x40e00000, v7
	v_mul_f32_e32 v10, 0xc01d265f, v6
	v_mul_f32_e32 v11, 0xc01d265f, v7
	v_exp_f32_e32 v10, v10
	v_exp_f32_e32 v11, v11
	v_pk_add_f32 v[14:15], v[14:15], 1.0 op_sel_hi:[1,0]
	v_pk_mul_f32 v[4:5], v[4:5], v[8:9]
	v_med3_f32 v12, v12, s71, v242
	v_med3_f32 v13, v13, s71, v242
	v_pk_mul_f32 v[4:5], v[4:5], v[14:15]
	v_mov_b32_e32 v8, v215
	v_cvt_pk_fp8_f32 v8, v4, v5
	v_pk_add_f32 v[4:5], v[12:13], 1.0 op_sel_hi:[1,0]
	v_pk_fma_f32 v[12:13], v[122:123], s[50:51], v[70:71] op_sel_hi:[1,0,1]
	v_add_f32_e32 v10, 1.0, v10
	v_add_f32_e32 v11, 1.0, v11
	v_min_f32_e32 v12, 0x40e00000, v12
	v_rcp_f32_e32 v10, v10
	v_rcp_f32_e32 v11, v11
	v_min_f32_e32 v13, 0x40e00000, v13
	v_mul_f32_e32 v9, 0xc01d265f, v12
	v_exp_f32_e32 v9, v9
	v_mul_f32_e32 v14, 0xc01d265f, v13
	v_exp_f32_e32 v15, v14
	v_pk_mul_f32 v[6:7], v[6:7], v[10:11]
	v_pk_fma_f32 v[10:11], v[124:125], s[50:51], v[72:73] op_sel_hi:[1,0,1]
	v_add_f32_e32 v9, 1.0, v9
	v_min_f32_e32 v10, 0x40e00000, v10
	v_min_f32_e32 v11, 0x40e00000, v11
	v_rcp_f32_e32 v14, v9
	v_add_f32_e32 v9, 1.0, v15
	v_mul_f32_e32 v15, 0xc01d265f, v10
	v_exp_f32_e32 v16, v15
	v_mul_f32_e32 v15, 0xc01d265f, v11
	v_exp_f32_e32 v17, v15
	v_rcp_f32_e32 v15, v9
	v_pk_mul_f32 v[4:5], v[6:7], v[4:5]
	v_pk_fma_f32 v[6:7], v[118:119], s[50:51], v[74:75] op_sel_hi:[1,0,1]
	v_add_f32_e32 v9, 1.0, v16
	v_med3_f32 v6, v6, s71, v242
	v_med3_f32 v7, v7, s71, v242
	v_rcp_f32_e32 v16, v9
	v_add_f32_e32 v9, 1.0, v17
	v_pk_add_f32 v[6:7], v[6:7], 1.0 op_sel_hi:[1,0]
	v_rcp_f32_e32 v17, v9
	v_pk_mul_f32 v[12:13], v[12:13], v[14:15]
	v_mov_b32_e32 v9, v215
	v_pk_mul_f32 v[6:7], v[12:13], v[6:7]
	v_cvt_pk_fp8_f32 v8, v4, v5 op_sel:[0,0,1]
	v_pk_fma_f32 v[4:5], v[120:121], s[50:51], v[76:77] op_sel_hi:[1,0,1]
	v_cvt_pk_fp8_f32 v9, v6, v7
	v_med3_f32 v4, v4, s71, v242
	v_med3_f32 v5, v5, s71, v242
	v_pk_add_f32 v[4:5], v[4:5], 1.0 op_sel_hi:[1,0]
	v_pk_mul_f32 v[6:7], v[10:11], v[16:17]
	s_mov_b32 s21, 0x24000
	v_pk_mul_f32 v[4:5], v[6:7], v[4:5]
	v_pk_fma_f32 v[14:15], v[110:111], s[50:51], v[82:83] op_sel_hi:[1,0,1]
	v_cvt_pk_fp8_f32 v9, v4, v5 op_sel:[0,0,1]
	v_add_co_u32_e32 v4, vcc, s21, v2
	v_med3_f32 v14, v14, s71, v242
	s_nop 0
	v_addc_co_u32_e32 v5, vcc, 0, v3, vcc
	global_store_dwordx2 v[4:5], v[8:9], off
	v_pk_fma_f32 v[4:5], v[114:115], s[50:51], v[78:79] op_sel_hi:[1,0,1]
	v_med3_f32 v15, v15, s71, v242
	v_min_f32_e32 v4, 0x40e00000, v4
	v_mul_f32_e32 v6, 0xc01d265f, v4
	v_min_f32_e32 v5, 0x40e00000, v5
	v_exp_f32_e32 v8, v6
	v_mul_f32_e32 v6, 0xc01d265f, v5
	v_exp_f32_e32 v9, v6
	v_pk_fma_f32 v[6:7], v[116:117], s[50:51], v[80:81] op_sel_hi:[1,0,1]
	v_add_f32_e32 v8, 1.0, v8
	v_rcp_f32_e32 v8, v8
	v_add_f32_e32 v9, 1.0, v9
	v_rcp_f32_e32 v9, v9
	v_min_f32_e32 v6, 0x40e00000, v6
	v_min_f32_e32 v7, 0x40e00000, v7
	v_mul_f32_e32 v10, 0xc01d265f, v6
	v_mul_f32_e32 v11, 0xc01d265f, v7
	v_exp_f32_e32 v10, v10
	v_exp_f32_e32 v11, v11
	v_pk_fma_f32 v[12:13], v[112:113], s[50:51], v[84:85] op_sel_hi:[1,0,1]
	v_pk_add_f32 v[14:15], v[14:15], 1.0 op_sel_hi:[1,0]
	v_pk_mul_f32 v[4:5], v[4:5], v[8:9]
	v_med3_f32 v12, v12, s71, v242
	v_med3_f32 v13, v13, s71, v242
	v_pk_mul_f32 v[4:5], v[4:5], v[14:15]
	v_mov_b32_e32 v8, v215
	v_cvt_pk_fp8_f32 v8, v4, v5
	v_pk_add_f32 v[4:5], v[12:13], 1.0 op_sel_hi:[1,0]
	v_pk_fma_f32 v[12:13], v[106:107], s[50:51], v[70:71] op_sel_hi:[1,0,1]
	v_add_f32_e32 v10, 1.0, v10
	v_add_f32_e32 v11, 1.0, v11
	v_min_f32_e32 v12, 0x40e00000, v12
	v_rcp_f32_e32 v10, v10
	v_rcp_f32_e32 v11, v11
	v_min_f32_e32 v13, 0x40e00000, v13
	v_mul_f32_e32 v9, 0xc01d265f, v12
	v_exp_f32_e32 v9, v9
	v_mul_f32_e32 v14, 0xc01d265f, v13
	v_exp_f32_e32 v15, v14
	v_pk_mul_f32 v[6:7], v[6:7], v[10:11]
	v_pk_fma_f32 v[10:11], v[108:109], s[50:51], v[72:73] op_sel_hi:[1,0,1]
	v_add_f32_e32 v9, 1.0, v9
	v_min_f32_e32 v10, 0x40e00000, v10
	v_min_f32_e32 v11, 0x40e00000, v11
	v_rcp_f32_e32 v14, v9
	v_add_f32_e32 v9, 1.0, v15
	v_mul_f32_e32 v15, 0xc01d265f, v10
	v_exp_f32_e32 v16, v15
	v_mul_f32_e32 v15, 0xc01d265f, v11
	v_exp_f32_e32 v17, v15
	v_rcp_f32_e32 v15, v9
	v_pk_mul_f32 v[4:5], v[6:7], v[4:5]
	v_pk_fma_f32 v[6:7], v[102:103], s[50:51], v[74:75] op_sel_hi:[1,0,1]
	v_add_f32_e32 v9, 1.0, v16
	v_med3_f32 v6, v6, s71, v242
	v_med3_f32 v7, v7, s71, v242
	v_rcp_f32_e32 v16, v9
	v_add_f32_e32 v9, 1.0, v17
	v_pk_add_f32 v[6:7], v[6:7], 1.0 op_sel_hi:[1,0]
	v_rcp_f32_e32 v17, v9
	v_pk_mul_f32 v[12:13], v[12:13], v[14:15]
	v_mov_b32_e32 v9, v215
	v_pk_mul_f32 v[6:7], v[12:13], v[6:7]
	v_cvt_pk_fp8_f32 v8, v4, v5 op_sel:[0,0,1]
	v_pk_fma_f32 v[4:5], v[104:105], s[50:51], v[76:77] op_sel_hi:[1,0,1]
	v_cvt_pk_fp8_f32 v9, v6, v7
	v_med3_f32 v4, v4, s71, v242
	v_med3_f32 v5, v5, s71, v242
	v_pk_add_f32 v[4:5], v[4:5], 1.0 op_sel_hi:[1,0]
	v_pk_mul_f32 v[6:7], v[10:11], v[16:17]
	s_mov_b32 s21, 0x28000
	v_pk_mul_f32 v[4:5], v[6:7], v[4:5]
	v_pk_fma_f32 v[10:11], v[98:99], s[50:51], v[78:79] op_sel_hi:[1,0,1]
	v_cvt_pk_fp8_f32 v9, v4, v5 op_sel:[0,0,1]
	v_add_co_u32_e32 v4, vcc, s21, v2
	v_min_f32_e32 v10, 0x40e00000, v10
	v_min_f32_e32 v11, 0x40e00000, v11
	v_addc_co_u32_e32 v5, vcc, 0, v3, vcc
	v_mul_f32_e32 v12, 0xc01d265f, v10
	v_mul_f32_e32 v13, 0xc01d265f, v11
	global_store_dwordx2 v[4:5], v[8:9], off
	v_pk_fma_f32 v[8:9], v[100:101], s[50:51], v[80:81] op_sel_hi:[1,0,1]
	v_exp_f32_e32 v12, v12
	v_exp_f32_e32 v13, v13
	v_min_f32_e32 v8, 0x40e00000, v8
	v_min_f32_e32 v9, 0x40e00000, v9
	v_mul_f32_e32 v14, 0xc01d265f, v8
	v_mul_f32_e32 v15, 0xc01d265f, v9
	v_exp_f32_e32 v14, v14
	v_exp_f32_e32 v15, v15
	v_add_f32_e32 v12, 1.0, v12
	v_add_f32_e32 v13, 1.0, v13
	v_rcp_f32_e32 v12, v12
	v_rcp_f32_e32 v13, v13
	v_add_f32_e32 v14, 1.0, v14
	v_add_f32_e32 v15, 1.0, v15
	v_pk_fma_f32 v[6:7], v[94:95], s[50:51], v[82:83] op_sel_hi:[1,0,1]
	v_rcp_f32_e32 v14, v14
	v_rcp_f32_e32 v15, v15
	v_med3_f32 v6, v6, s71, v242
	v_med3_f32 v7, v7, s71, v242
	v_pk_mul_f32 v[10:11], v[10:11], v[12:13]
	v_pk_fma_f32 v[12:13], v[90:91], s[50:51], v[70:71] op_sel_hi:[1,0,1]
	v_pk_add_f32 v[6:7], v[6:7], 1.0 op_sel_hi:[1,0]
	v_min_f32_e32 v12, 0x40e00000, v12
	v_pk_mul_f32 v[6:7], v[10:11], v[6:7]
	v_mov_b32_e32 v10, v215
	v_min_f32_e32 v13, 0x40e00000, v13
	v_mul_f32_e32 v11, 0xc01d265f, v12
	v_cvt_pk_fp8_f32 v10, v6, v7
	v_pk_mul_f32 v[6:7], v[8:9], v[14:15]
	v_exp_f32_e32 v11, v11
	v_mul_f32_e32 v14, 0xc01d265f, v13
	v_exp_f32_e32 v15, v14
	v_pk_fma_f32 v[8:9], v[92:93], s[50:51], v[72:73] op_sel_hi:[1,0,1]
	v_add_f32_e32 v11, 1.0, v11
	v_min_f32_e32 v8, 0x40e00000, v8
	v_min_f32_e32 v9, 0x40e00000, v9
	v_rcp_f32_e32 v14, v11
	v_add_f32_e32 v11, 1.0, v15
	v_mul_f32_e32 v15, 0xc01d265f, v8
	v_exp_f32_e32 v16, v15
	v_mul_f32_e32 v15, 0xc01d265f, v9
	v_pk_fma_f32 v[4:5], v[96:97], s[50:51], v[84:85] op_sel_hi:[1,0,1]
	v_exp_f32_e32 v17, v15
	v_med3_f32 v4, v4, s71, v242
	v_med3_f32 v5, v5, s71, v242
	v_rcp_f32_e32 v15, v11
	v_pk_add_f32 v[4:5], v[4:5], 1.0 op_sel_hi:[1,0]
	v_add_f32_e32 v11, 1.0, v16
	v_pk_mul_f32 v[4:5], v[6:7], v[4:5]
	v_pk_fma_f32 v[6:7], v[86:87], s[50:51], v[74:75] op_sel_hi:[1,0,1]
	v_rcp_f32_e32 v16, v11
	v_med3_f32 v6, v6, s71, v242
	v_med3_f32 v7, v7, s71, v242
	v_add_f32_e32 v11, 1.0, v17
	v_pk_add_f32 v[6:7], v[6:7], 1.0 op_sel_hi:[1,0]
	v_rcp_f32_e32 v17, v11
	v_pk_mul_f32 v[12:13], v[12:13], v[14:15]
	v_mov_b32_e32 v11, v215
	v_pk_mul_f32 v[6:7], v[12:13], v[6:7]
	v_cvt_pk_fp8_f32 v10, v4, v5 op_sel:[0,0,1]
	v_pk_fma_f32 v[4:5], v[88:89], s[50:51], v[76:77] op_sel_hi:[1,0,1]
	v_cvt_pk_fp8_f32 v11, v6, v7
	v_med3_f32 v4, v4, s71, v242
	v_med3_f32 v5, v5, s71, v242
	v_pk_add_f32 v[4:5], v[4:5], 1.0 op_sel_hi:[1,0]
	v_pk_mul_f32 v[6:7], v[8:9], v[16:17]
	v_add_co_u32_e32 v2, vcc, 0x2c000, v2
	v_pk_mul_f32 v[4:5], v[6:7], v[4:5]
	s_nop 0
	v_addc_co_u32_e32 v3, vcc, 0, v3, vcc
	v_cvt_pk_fp8_f32 v11, v4, v5 op_sel:[0,0,1]
	s_and_b64 vcc, exec, s[4:5]
	s_mov_b64 s[4:5], -1
	global_store_dwordx2 v[2:3], v[10:11], off
	s_cmp_eq_u32 s32, 0
	s_cbranch_scc1 .Lcg_skip_f
	s_waitcnt vmcnt(8)
	s_mov_b32 s100, 0x42800000
	s_mov_b32 s101, 0x42800000
	v_pk_mul_f32 v[24:25], v[24:25], s[100:101]
	v_pk_mul_f32 v[26:27], v[26:27], s[100:101]
	v_pk_mul_f32 v[28:29], v[28:29], s[100:101]
	v_pk_mul_f32 v[30:31], v[30:31], s[100:101]
	v_pk_mul_f32 v[32:33], v[32:33], s[100:101]
	v_pk_mul_f32 v[34:35], v[34:35], s[100:101]
	v_pk_mul_f32 v[36:37], v[36:37], s[100:101]
	v_pk_mul_f32 v[38:39], v[38:39], s[100:101]
	v_cvt_pk_fp8_f32 v24, v24, v28
	v_cvt_pk_fp8_f32 v24, v32, v36 op_sel:[0,0,1]
	v_cvt_pk_fp8_f32 v25, v25, v29
	v_cvt_pk_fp8_f32 v25, v33, v37 op_sel:[0,0,1]
	v_cvt_pk_fp8_f32 v26, v26, v30
	v_cvt_pk_fp8_f32 v26, v34, v38 op_sel:[0,0,1]
	v_cvt_pk_fp8_f32 v27, v27, v31
	v_cvt_pk_fp8_f32 v27, v35, v39 op_sel:[0,0,1]
	v_readfirstlane_b32 s84, v0
	s_lshr_b32 s84, s84, 6
	s_mul_i32 s85, s84, 0x440
	s_add_i32 s85, s85, s53
	s_add_i32 s85, s85, 0x20800
	s_cmp_lt_u32 s84, 5
	s_cselect_b32 s84, 0, 0x4ac0
	s_add_i32 s85, s85, s84
	v_and_b32_e32 v59, 63, v0
	v_and_b32_e32 v60, 3, v59
	v_mul_u32_u24_e32 v60, 0x44, v60
	v_lshrrev_b32_e32 v61, 2, v59
	v_add_u32_e32 v60, v60, v61
	v_lshl_add_u32 v60, v60, 2, s85
	v_mul_u32_u24_e32 v61, 17, v61
	v_and_b32_e32 v62, 3, v59
	v_lshl_add_u32 v61, v62, 2, v61
	v_lshl_add_u32 v61, v61, 2, s85
	v_lshrrev_b32_e32 v58, 2, v59
	v_lshlrev_b32_e32 v58, 10, v58
	v_lshl_or_b32 v58, v62, 4, v58
	ds_write2_b32 v60, v24, v25 offset1:17
	ds_write2_b32 v60, v26, v27 offset0:34 offset1:51
	s_waitcnt lgkmcnt(0)
	ds_read2_b32 v[28:29], v61 offset1:1
	ds_read2_b32 v[30:31], v61 offset0:2 offset1:3
	s_waitcnt lgkmcnt(0)
	global_store_dwordx4 v58, v[28:31], s[82:83] sc1 nt
